# variant: nt policy on the cached-block loads
# baseline (speedup 1.0000x reference)
.LBB3_6:
	s_xor_b32 s33, s32, 0xff
	s_add_i32 s33, s33, s24
	s_ashr_i32 s26, s33, 8
	v_cmp_gt_i32_e32 vcc, s24, v176
	v_med3_i32 v33, s26, 0, 6
	s_sub_i32 s33, s24, 0x100
	v_cmp_gt_i32_e64 s[4:5], s33, v176
	s_sub_i32 s33, s24, 0x200
	v_cmp_gt_i32_e64 s[6:7], s33, v176
	s_sub_i32 s33, s24, 0x300
	v_cmp_gt_i32_e64 s[8:9], s33, v176
	s_sub_i32 s33, s24, 0x400
	v_cmp_gt_i32_e64 s[10:11], s33, v176
	s_sub_i32 s33, s24, 0x500
	v_cmp_gt_i32_e64 s[12:13], s33, v176
	s_and_b32 s25, s25, 0x7ffff000
	s_mov_b32 s2, 0xffff0000
	v_readfirstlane_b32 s26, v33
	s_nop 3
	s_cmp_lt_i32 s26, 4
	s_waitcnt vmcnt(5)
	v_cndmask_b32_e32 v4, v29, v4, vcc
	v_cndmask_b32_e64 v134, v3, v2, s[0:1]
	v_cndmask_b32_e32 v134, 0, v134, vcc
	s_waitcnt vmcnt(4)
	v_cndmask_b32_e64 v3, v29, v8, s[4:5]
	v_cndmask_b32_e64 v97, v7, v6, s[0:1]
	v_cndmask_b32_e64 v97, 0, v97, s[4:5]
	v_cndmask_b32_e64 v135, 1.0, v4, s[0:1]
	v_cndmask_b32_e64 v33, -1, v9, s[4:5]
	v_cndmask_b32_e64 v98, 1.0, v3, s[0:1]
	s_waitcnt vmcnt(3)
	v_cndmask_b32_e64 v6, v29, v12, s[6:7]
	v_cndmask_b32_e64 v68, v11, v10, s[0:1]
	v_cndmask_b32_e64 v68, 0, v68, s[6:7]
	s_waitcnt vmcnt(2)
	v_cndmask_b32_e64 v7, v29, v16, s[8:9]
	v_cndmask_b32_e64 v70, 1.0, v6, s[0:1]
	v_cndmask_b32_e64 v73, 1.0, v7, s[0:1]
	v_cndmask_b32_e64 v34, -1, v13, s[6:7]
	v_cndmask_b32_e64 v35, -1, v17, s[8:9]
	v_cndmask_b32_e64 v71, v15, v14, s[0:1]
	v_cndmask_b32_e64 v71, 0, v71, s[8:9]
	s_waitcnt vmcnt(1)
	v_cndmask_b32_e64 v8, v29, v20, s[10:11]
	v_cndmask_b32_e64 v48, 1.0, v8, s[0:1]
	s_waitcnt vmcnt(0)
	v_cndmask_b32_e64 v10, v29, v24, s[12:13]
	v_cndmask_b32_e32 v29, -1, v5, vcc
	v_max_i32_e32 v4, 0, v29
	v_add_u32_e32 v4, s25, v4
	v_mov_b32_e32 v5, 0
	v_lshl_add_u64 v[6:7], v[4:5], 2, s[16:17]
	v_max_i32_e32 v4, 0, v33
	v_add_u32_e32 v4, s25, v4
	v_lshl_add_u64 v[8:9], v[4:5], 2, s[16:17]
	v_max_i32_e32 v4, 0, v34
	v_add_u32_e32 v4, s25, v4
	v_cndmask_b32_e64 v3, 1.0, v10, s[0:1]
	v_lshl_add_u64 v[10:11], v[4:5], 2, s[16:17]
	v_max_i32_e32 v4, 0, v35
	v_cndmask_b32_e64 v36, -1, v21, s[10:11]
	v_add_u32_e32 v4, s25, v4
	v_lshl_add_u64 v[12:13], v[4:5], 2, s[16:17]
	v_max_i32_e32 v4, 0, v36
	v_cndmask_b32_e64 v37, -1, v25, s[12:13]
	v_add_u32_e32 v4, s25, v4
	v_lshl_add_u64 v[14:15], v[4:5], 2, s[16:17]
	v_max_i32_e32 v4, 0, v37
	v_cndmask_b32_e64 v46, v19, v18, s[0:1]
	v_cndmask_b32_e64 v46, 0, v46, s[10:11]
	v_cndmask_b32_e64 v2, v23, v22, s[0:1]
	v_cndmask_b32_e64 v2, 0, v2, s[12:13]
	v_add_u32_e32 v4, s25, v4
	v_lshl_add_u64 v[4:5], v[4:5], 2, s[16:17]
	s_cmpk_lt_i32 s24, 0x801
	s_cselect_b32 s47, 1, 0
	s_cbranch_scc0 .Lffc_nocache
	s_lshl_b32 s46, s27, 12
	s_add_u32 s46, s46, 0x8000
	s_add_u32 s44, s20, s46
	s_addc_u32 s45, s21, 0
	v_lshlrev_b32_e32 v183, 4, v38
	global_load_dwordx4 v[184:187], v183, s[44:45] nt
	global_load_dwordx4 v[188:191], v183, s[44:45] offset:1024 nt
	global_load_dwordx4 v[192:195], v183, s[44:45] offset:2048 nt
	global_load_dwordx4 v[196:199], v183, s[44:45] offset:3072 nt

.LBB4_6:
	s_xor_b32 s33, s32, 0xff
	s_add_i32 s33, s33, s26
	s_ashr_i32 s27, s33, 8
	v_cmp_gt_i32_e32 vcc, s26, v176
	v_med3_i32 v33, s27, 0, 6
	s_sub_i32 s33, s26, 0x100
	v_cmp_gt_i32_e64 s[4:5], s33, v176
	s_sub_i32 s33, s26, 0x200
	v_cmp_gt_i32_e64 s[6:7], s33, v176
	s_sub_i32 s33, s26, 0x300
	v_cmp_gt_i32_e64 s[8:9], s33, v176
	s_sub_i32 s33, s26, 0x400
	v_cmp_gt_i32_e64 s[10:11], s33, v176
	s_sub_i32 s33, s26, 0x500
	v_cmp_gt_i32_e64 s[12:13], s33, v176
	s_and_b32 s27, s29, 0x7ffff000
	s_mov_b32 s2, 0xffff0000
	v_readfirstlane_b32 s28, v33
	s_nop 3
	s_cmp_lt_i32 s28, 4
	s_waitcnt vmcnt(5)
	v_cndmask_b32_e32 v4, v29, v4, vcc
	v_cndmask_b32_e64 v134, v3, v2, s[0:1]
	v_cndmask_b32_e32 v134, 0, v134, vcc
	s_waitcnt vmcnt(4)
	v_cndmask_b32_e64 v3, v29, v8, s[4:5]
	v_cndmask_b32_e64 v97, v7, v6, s[0:1]
	v_cndmask_b32_e64 v97, 0, v97, s[4:5]
	v_cndmask_b32_e64 v135, 1.0, v4, s[0:1]
	v_cndmask_b32_e64 v33, -1, v9, s[4:5]
	v_cndmask_b32_e64 v98, 1.0, v3, s[0:1]
	s_waitcnt vmcnt(3)
	v_cndmask_b32_e64 v6, v29, v12, s[6:7]
	v_cndmask_b32_e64 v68, v11, v10, s[0:1]
	v_cndmask_b32_e64 v68, 0, v68, s[6:7]
	s_waitcnt vmcnt(2)
	v_cndmask_b32_e64 v7, v29, v16, s[8:9]
	v_cndmask_b32_e64 v70, 1.0, v6, s[0:1]
	v_cndmask_b32_e64 v73, 1.0, v7, s[0:1]
	v_cndmask_b32_e64 v34, -1, v13, s[6:7]
	v_cndmask_b32_e64 v35, -1, v17, s[8:9]
	v_cndmask_b32_e64 v71, v15, v14, s[0:1]
	v_cndmask_b32_e64 v71, 0, v71, s[8:9]
	s_waitcnt vmcnt(1)
	v_cndmask_b32_e64 v8, v29, v20, s[10:11]
	v_cndmask_b32_e64 v48, 1.0, v8, s[0:1]
	s_waitcnt vmcnt(0)
	v_cndmask_b32_e64 v10, v29, v24, s[12:13]
	v_cndmask_b32_e32 v29, -1, v5, vcc
	v_max_i32_e32 v4, 0, v29
	v_add_u32_e32 v4, s27, v4
	v_mov_b32_e32 v5, 0
	v_lshl_add_u64 v[6:7], v[4:5], 2, s[16:17]
	v_max_i32_e32 v4, 0, v33
	v_add_u32_e32 v4, s27, v4
	v_lshl_add_u64 v[8:9], v[4:5], 2, s[16:17]
	v_max_i32_e32 v4, 0, v34
	v_add_u32_e32 v4, s27, v4
	v_cndmask_b32_e64 v3, 1.0, v10, s[0:1]
	v_lshl_add_u64 v[10:11], v[4:5], 2, s[16:17]
	v_max_i32_e32 v4, 0, v35
	v_cndmask_b32_e64 v36, -1, v21, s[10:11]
	v_add_u32_e32 v4, s27, v4
	v_lshl_add_u64 v[12:13], v[4:5], 2, s[16:17]
	v_max_i32_e32 v4, 0, v36
	v_cndmask_b32_e64 v37, -1, v25, s[12:13]
	v_add_u32_e32 v4, s27, v4
	v_lshl_add_u64 v[14:15], v[4:5], 2, s[16:17]
	v_max_i32_e32 v4, 0, v37
	v_cndmask_b32_e64 v46, v19, v18, s[0:1]
	v_cndmask_b32_e64 v46, 0, v46, s[10:11]
	v_cndmask_b32_e64 v2, v23, v22, s[0:1]
	v_cndmask_b32_e64 v2, 0, v2, s[12:13]
	v_add_u32_e32 v4, s27, v4
	v_lshl_add_u64 v[4:5], v[4:5], 2, s[16:17]
	s_cmpk_lt_i32 s26, 0x801
	s_cselect_b32 s47, 1, 0
	s_cbranch_scc0 .Lftc_nocache
	s_lshl_b32 s46, s30, 12
	s_add_u32 s46, s46, 0x8000
	s_add_u32 s44, s20, s46
	s_addc_u32 s45, s21, 0
	v_lshlrev_b32_e32 v183, 4, v38
	global_load_dwordx4 v[184:187], v183, s[44:45] nt
	global_load_dwordx4 v[188:191], v183, s[44:45] offset:1024 nt
	global_load_dwordx4 v[192:195], v183, s[44:45] offset:2048 nt
	global_load_dwordx4 v[196:199], v183, s[44:45] offset:3072 nt
